# i4 + grid barrier arrival: arrival atomic issued before the early invalidate and the wait for its return value no longer covers the invalidate (counted vmcnt)
# baseline (speedup 1.0000x reference)
.LBB0_764:
	v_readlane_b32 s4, v243, 61
	v_readlane_b32 s5, v243, 62
	v_cvt_f32_u32_e32 v1, v4
	v_sub_u32_e32 v6, 0, v4
	v_rcp_iflag_f32_e32 v1, v1
	s_nop 1
	global_atomic_add v5, v3, v216, s[4:5] sc0
	buffer_inv sc1
	v_mul_f32_e32 v1, 0x4f7ffffe, v1
	v_cvt_u32_f32_e32 v1, v1
	v_mul_lo_u32 v6, v6, v1
	v_mul_hi_u32 v6, v1, v6
	v_add_u32_e32 v1, v1, v6
	s_waitcnt vmcnt(1)
	v_mul_hi_u32 v1, v5, v1
	v_mul_lo_u32 v6, v1, v4
	v_sub_u32_e32 v6, v5, v6
	v_add_u32_e32 v7, 1, v1
	v_cmp_ge_u32_e32 vcc, v6, v4
	v_add_u32_e32 v5, 1, v5
	s_nop 0
	v_cndmask_b32_e32 v1, v1, v7, vcc
	v_sub_u32_e32 v7, v6, v4
	v_cndmask_b32_e32 v6, v6, v7, vcc
	v_add_u32_e32 v7, 1, v1
	v_cmp_ge_u32_e32 vcc, v6, v4
	s_nop 1
	v_cndmask_b32_e32 v1, v1, v7, vcc
	v_mul_lo_u32 v6, v4, v1
	v_add_u32_e32 v4, v6, v4
	v_cmp_ne_u32_e32 vcc, v5, v4
	s_and_saveexec_b64 s[4:5], vcc
	s_xor_b64 s[4:5], exec, s[4:5]
	s_cbranch_execz .LBB0_778
	s_waitcnt lgkmcnt(0)
	v_readlane_b32 s98, v242, 1
	v_readlane_b32 s99, v242, 2
	s_nop 4
	global_load_dword v2, v3, s[98:99] sc1
	s_waitcnt vmcnt(0)
	v_cmp_eq_u32_e32 vcc, v2, v1
	s_and_saveexec_b64 s[6:7], vcc
	s_cbranch_execz .LBB0_777
	s_mov_b32 s19, 1
	s_mov_b64 s[8:9], 0
	s_branch .LBB0_768

.LBB0_2938:
	v_readlane_b32 s4, v243, 61
	v_readlane_b32 s5, v243, 62
	v_cvt_f32_u32_e32 v1, v4
	v_sub_u32_e32 v6, 0, v4
	v_rcp_iflag_f32_e32 v1, v1
	s_nop 1
	global_atomic_add v5, v3, v216, s[4:5] sc0
	buffer_inv sc1
	v_mul_f32_e32 v1, 0x4f7ffffe, v1
	v_cvt_u32_f32_e32 v1, v1
	v_mul_lo_u32 v6, v6, v1
	v_mul_hi_u32 v6, v1, v6
	v_add_u32_e32 v1, v1, v6
	s_waitcnt vmcnt(1)
	v_mul_hi_u32 v1, v5, v1
	v_mul_lo_u32 v6, v1, v4
	v_sub_u32_e32 v6, v5, v6
	v_add_u32_e32 v7, 1, v1
	v_cmp_ge_u32_e32 vcc, v6, v4
	v_add_u32_e32 v5, 1, v5
	s_nop 0
	v_cndmask_b32_e32 v1, v1, v7, vcc
	v_sub_u32_e32 v7, v6, v4
	v_cndmask_b32_e32 v6, v6, v7, vcc
	v_add_u32_e32 v7, 1, v1
	v_cmp_ge_u32_e32 vcc, v6, v4
	s_nop 1
	v_cndmask_b32_e32 v1, v1, v7, vcc
	v_mul_lo_u32 v6, v4, v1
	v_add_u32_e32 v4, v6, v4
	v_cmp_ne_u32_e32 vcc, v5, v4
	s_and_saveexec_b64 s[4:5], vcc
	s_xor_b64 s[4:5], exec, s[4:5]
	s_cbranch_execz .LBB0_2952
	s_waitcnt lgkmcnt(0)
	v_readlane_b32 s98, v242, 1
	v_readlane_b32 s99, v242, 2
	s_nop 4
	global_load_dword v2, v3, s[98:99] sc1
	s_waitcnt vmcnt(0)
	v_cmp_eq_u32_e32 vcc, v2, v1
	s_and_saveexec_b64 s[6:7], vcc
	s_cbranch_execz .LBB0_2951
	s_mov_b32 s18, 1
	s_mov_b64 s[8:9], 0
	s_branch .LBB0_2942
